# v5 + next-unit index of the z and up GEMMs computed directly (pm same, pn+4) when grid is 256 instead of the generic division
# speedup vs baseline: 1.0090x; 1.0013x over previous
.LBB0_496:
	s_add_i32 s95, s95, 1
	s_cmpk_eq_i32 s48, 0x100
	s_cbranch_scc0 .Lz_gen_next
	s_add_i32 s22, s8, 4
	s_mov_b32 s24, s14
	s_cmpk_lt_i32 s22, 12
	s_cselect_b64 s[6:7], -1, 0
	s_branch .LBB0_498
.Lz_gen_next:
	s_mul_i32 s6, s95, s82
	s_mul_hi_u32 s7, s95, s48
	s_add_i32 s7, s7, s6
	s_mul_i32 s6, s95, s48
	s_add_u32 s26, s6, s2
	s_addc_u32 s27, s7, s3
	v_cmp_gt_i64_e32 vcc, s[26:27], v[156:157]
	v_cmp_lt_i64_e64 s[6:7], s[26:27], v[154:155]
	s_cbranch_vccnz .LBB0_498
	s_ashr_i32 s9, s26, 31
	s_lshr_b32 s9, s9, 29
	s_add_i32 s9, s26, s9
	s_ashr_i32 s22, s9, 3
	s_and_b32 s9, s9, -8
	s_sub_i32 s9, s26, s9
	s_cmp_lt_i32 s9, 0
	s_cselect_b32 s23, s84, 0x60
	s_mul_i32 s9, s9, s23
	s_add_i32 s9, s9, s22
	s_mul_hi_i32 s22, s9, 0x2aaaaaab
	s_lshr_b32 s23, s22, 31
	s_ashr_i32 s22, s22, 4
	s_add_i32 s22, s22, s23
	s_lshl_b32 s23, s22, 3
	s_sub_i32 s24, 64, s23
	s_min_i32 s24, s24, 8
	s_abs_i32 s25, s24
	v_cvt_f32_u32_e32 v2, s25
	s_sub_i32 s27, 0, s25
	s_mulk_i32 s22, 0x60
	s_sub_i32 s9, s9, s22
	v_rcp_iflag_f32_e32 v2, v2
	s_abs_i32 s22, s9
	s_xor_b32 s26, s9, s24
	s_ashr_i32 s26, s26, 31
	v_mul_f32_e32 v2, 0x4f7ffffe, v2
	v_cvt_u32_f32_e32 v2, v2
	s_nop 0
	v_readfirstlane_b32 s28, v2
	s_mul_i32 s27, s27, s28
	s_mul_hi_u32 s27, s28, s27
	s_add_i32 s28, s28, s27
	s_mul_hi_u32 s27, s22, s28
	s_mul_i32 s28, s27, s25
	s_sub_i32 s22, s22, s28
	s_add_i32 s29, s27, 1
	s_sub_i32 s28, s22, s25
	s_cmp_ge_u32 s22, s25
	s_cselect_b32 s27, s29, s27
	s_cselect_b32 s22, s28, s22
	s_add_i32 s28, s27, 1
	s_cmp_ge_u32 s22, s25
	s_cselect_b32 s22, s28, s27
	s_xor_b32 s22, s22, s26
	s_sub_i32 s22, s22, s26
	s_mul_i32 s24, s22, s24
	s_sub_i32 s9, s9, s24
	s_add_i32 s24, s23, s9

.LBB0_1878:
	s_add_i32 s85, s85, 1
	s_cmpk_eq_i32 s48, 0x100
	s_cbranch_scc0 .Lup_gen_next
	s_add_i32 s22, s30, 4
	s_mov_b32 s24, s34
	s_cmpk_lt_i32 s22, 16
	s_cselect_b64 s[4:5], -1, 0
	s_branch .LBB0_1884
.Lup_gen_next:
	s_mul_i32 s4, s85, s86
	s_mul_hi_u32 s5, s85, s48
	s_add_i32 s5, s5, s4
	s_mul_i32 s4, s85, s48
	s_add_u32 s26, s4, s2
	s_addc_u32 s27, s5, s3
	v_cmp_gt_i64_e32 vcc, s[26:27], v[140:141]
	v_cmp_lt_i64_e64 s[4:5], s[26:27], v[138:139]
	s_cbranch_vccnz .LBB0_1884
	s_ashr_i32 s22, s26, 31
	s_lshr_b32 s22, s22, 29
	s_add_i32 s24, s26, s22
	s_and_b32 s22, s24, -8
	s_sub_i32 s25, s26, s22
	s_cmp_gt_i32 s25, -1
	s_mov_b64 s[22:23], -1
	s_cbranch_scc0 .LBB0_1881
	s_lshl_b32 s26, s25, 7
	s_mov_b64 s[22:23], 0
